# same as previous (arrival counters instead of grid barrier 3) with a larger bounded-spin cap
# baseline (speedup 1.0000x reference)
; __global__ void __launch_bounds__(512, 2) hymba_fwd(Args args) {
;     ...
;             __syncthreads();
;             for (int idx = tid; idx < 32 * 48; idx += 512) { float a = 0.f;
; #pragma unroll
;                 for (int w8 = 0; w8 < 8; ++w8) a += part[w8 * 1536 + idx];
;                 logit[idx] = a; }
.Lms_spin:
	global_load_dword v1, v0, s[20:21] sc0 sc1
	s_waitcnt vmcnt(0)
	v_readfirstlane_b32 s17, v1
	s_cmp_ge_u32 s17, 8
	s_cbranch_scc1 .Lms_done
	s_sleep 2
	s_add_i32 s16, s16, 1
	s_cmpk_lt_u32 s16, 0x4000
	s_cbranch_scc1 .Lms_spin
